# baseline (speedup 1.0000x reference)
.LBB5_134:
	s_or_b64 exec, exec, s[12:13]
	v_mov_b32_e32 v1, 0
	s_and_b64 vcc, exec, s[0:1]
	v_lshlrev_b32_e32 v131, 2, v131
	s_cbranch_vccnz .LBB5_138
	v_mov_b32_e32 v0, 0x23e90
	ds_read_b64 v[30:31], v0
	v_mov_b32_e32 v38, 0x3000
	v_lshl_or_b32 v165, v128, 4, v38
	v_mov_b32_e32 v38, 0x9000
	v_lshl_or_b32 v164, v128, 3, v38
	v_or_b32_e32 v166, 0x23900, v131
	v_lshlrev_b32_e32 v167, 2, v127
	v_or_b32_e32 v167, 0x23b00, v167
	v_mov_b32_e32 v94, 0xf149f2ca
	v_mov_b32_e32 v62, 0x3fb8aa3b
	v_mov_b32_e32 v63, 0x3fb8aa3b
	ds_read_b128 v[42:45], v166 offset:768
	ds_read_b128 v[50:53], v166 offset:832
	ds_read_b128 v[58:61], v166 offset:896
	ds_read_b128 v[66:69], v166 offset:960
	ds_read_b128 v[38:41], v166
	ds_read_b128 v[46:49], v166 offset:256
	ds_read_b128 v[132:135], v165
	ds_read_b128 v[136:139], v165 offset:1024
	ds_read_b128 v[140:143], v165 offset:8192
	ds_read_b128 v[144:147], v165 offset:9216
	s_waitcnt lgkmcnt(10)
	v_pk_add_f32 v[0:1], v[120:121], v[30:31] op_sel_hi:[1,0] neg_lo:[0,1] neg_hi:[0,1]
	v_pk_add_f32 v[32:33], v[122:123], v[30:31] op_sel_hi:[1,0] neg_lo:[0,1] neg_hi:[0,1]
	v_pk_mul_f32 v[0:1], v[30:31], v[0:1] op_sel:[1,0]
	v_pk_mul_f32 v[32:33], v[30:31], v[32:33] op_sel:[1,0]
	v_pk_fma_f32 v[84:85], v[70:71], v[0:1], v[102:103]
	v_pk_fma_f32 v[0:1], v[72:73], v[32:33], v[104:105]
	v_pk_add_f32 v[32:33], v[118:119], v[30:31] op_sel_hi:[1,0] neg_lo:[0,1] neg_hi:[0,1]
	v_pk_mul_f32 v[32:33], v[30:31], v[32:33] op_sel:[1,0]
	v_pk_fma_f32 v[118:119], v[74:75], v[32:33], v[106:107]
	v_pk_add_f32 v[32:33], v[124:125], v[30:31] op_sel_hi:[1,0] neg_lo:[0,1] neg_hi:[0,1]
	v_pk_mul_f32 v[32:33], v[30:31], v[32:33] op_sel:[1,0]
	v_pk_fma_f32 v[124:125], v[76:77], v[32:33], v[108:109]
	v_pk_add_f32 v[32:33], v[116:117], v[30:31] op_sel_hi:[1,0] neg_lo:[0,1] neg_hi:[0,1]
	v_pk_mul_f32 v[32:33], v[30:31], v[32:33] op_sel:[1,0]
	v_pk_fma_f32 v[116:117], v[96:97], v[32:33], v[86:87]
	v_pk_add_f32 v[32:33], v[114:115], v[30:31] op_sel_hi:[1,0] neg_lo:[0,1] neg_hi:[0,1]
	v_cvt_pk_bf16_f32 v34, v116, v117
	v_pk_mul_f32 v[32:33], v[30:31], v[32:33] op_sel:[1,0]
	v_cmp_eq_u32_e32 vcc, 3, v126
	v_pk_fma_f32 v[114:115], v[152:153], v[32:33], v[88:89]
	v_pk_add_f32 v[32:33], v[110:111], v[30:31] op_sel_hi:[1,0] neg_lo:[0,1] neg_hi:[0,1]
	v_cvt_pk_bf16_f32 v35, v114, v115
	v_pk_mul_f32 v[32:33], v[30:31], v[32:33] op_sel:[1,0]
	v_pk_fma_f32 v[110:111], v[90:91], v[32:33], v[98:99]
	v_pk_add_f32 v[32:33], v[112:113], v[30:31] op_sel_hi:[1,0] neg_lo:[0,1] neg_hi:[0,1]
	v_cvt_pk_bf16_f32 v36, v110, v111
	v_pk_mul_f32 v[30:31], v[30:31], v[32:33] op_sel:[1,0]
	v_cvt_pk_bf16_f32 v32, v118, v119
	v_pk_fma_f32 v[112:113], v[92:93], v[30:31], v[100:101]
	v_cvt_pk_bf16_f32 v30, v84, v85
	v_cvt_pk_bf16_f32 v31, v0, v1
	v_cvt_pk_bf16_f32 v33, v124, v125
	v_cvt_pk_bf16_f32 v37, v112, v113
	ds_read2_b32 v[54:55], v167 offset0:0 offset1:0
	ds_read2_b32 v[56:57], v167 offset0:0 offset1:0
	ds_read_b128 v[148:151], v165 offset:16384
	ds_read_b128 v[154:157], v165 offset:17408
	ds_read2st64_b64 v[96:99], v164 offset0:0 offset1:1
	ds_read2st64_b64 v[100:103], v164 offset0:4 offset1:5
	ds_read2st64_b64 v[104:107], v164 offset0:8 offset1:9
	ds_read2st64_b64 v[160:163], v164 offset0:12 offset1:13
	s_waitcnt lgkmcnt(4)
	v_mfma_f32_16x16x32_bf16 v[38:41], v[132:135], v[30:33], v[38:41]
	v_mfma_f32_16x16x32_bf16 v[46:49], v[140:143], v[30:33], v[46:49]
	v_mfma_f32_16x16x32_bf16 v[54:57], v[30:33], v[148:151], v[54:57]
	v_mfma_f32_16x16x32_bf16 v[38:41], v[136:139], v[34:37], v[38:41]
	v_mfma_f32_16x16x32_bf16 v[46:49], v[144:147], v[34:37], v[46:49]
	v_mfma_f32_16x16x32_bf16 v[54:57], v[34:37], v[154:157], v[54:57]
	ds_read_b128 v[132:135], v165 offset:2048
	ds_read_b128 v[136:139], v165 offset:3072
	ds_read_b128 v[140:143], v165 offset:10240
	ds_read_b128 v[144:147], v165 offset:11264
	ds_read_b128 v[148:151], v165 offset:18432
	ds_read_b128 v[154:157], v165 offset:19456
	s_nop 0
	v_cvt_pk_bf16_f32 v74, v38, v39
	v_cvt_pk_bf16_f32 v75, v40, v41
	v_cvt_pk_bf16_f32 v76, v46, v47
	v_cvt_pk_bf16_f32 v77, v48, v49
	ds_read_b128 v[38:41], v166 offset:64
	ds_read_b128 v[46:49], v166 offset:320
	v_mfma_f32_16x16x16_bf16 v[70:73], v[76:77], v[74:75], 0
	v_cvt_pk_bf16_f32 v86, v54, v55
	v_cvt_pk_bf16_f32 v87, v56, v57
	ds_read2_b32 v[54:55], v167 offset0:16 offset1:16
	ds_read2_b32 v[56:57], v167 offset0:16 offset1:16
	s_nop 3
	v_max_f32_e32 v88, v72, v73
	v_max3_f32 v88, v70, v71, v88
	v_cndmask_b32_e32 v88, v88, v94, vcc
	v_mov_b32_e32 v89, v88
	s_nop 1
	v_permlane16_swap_b32_e32 v88, v89
	v_max_f32_e32 v88, v88, v89
	v_mov_b32_e32 v89, v88
	s_nop 1
	v_permlane32_swap_b32_e32 v88, v89
	v_max_f32_e32 v88, v88, v89
	v_pk_add_f32 v[70:71], v[70:71], v[88:89] op_sel_hi:[1,0] neg_lo:[0,1] neg_hi:[0,1]
	v_pk_add_f32 v[72:73], v[72:73], v[88:89] op_sel_hi:[1,0] neg_lo:[0,1] neg_hi:[0,1]
	v_pk_mul_f32 v[70:71], v[62:63], v[70:71]
	v_pk_mul_f32 v[72:73], v[62:63], v[72:73]
	v_exp_f32_e32 v70, v70
	v_exp_f32_e32 v71, v71
	v_exp_f32_e32 v72, v72
	v_exp_f32_e32 v73, v73
	s_nop 0
	v_cndmask_b32_e64 v70, v70, 0, vcc
	v_cndmask_b32_e64 v71, v71, 0, vcc
	v_cndmask_b32_e64 v72, v72, 0, vcc
	v_cndmask_b32_e64 v73, v73, 0, vcc
	v_add_f32_e32 v90, v70, v71
	v_add_f32_e32 v91, v72, v73
	v_add_f32_e32 v90, v90, v91
	v_cvt_pk_bf16_f32 v92, v70, v71
	v_cvt_pk_bf16_f32 v93, v72, v73
	v_mov_b32_e32 v91, v90
	s_nop 1
	v_permlane16_swap_b32_e32 v90, v91
	v_add_f32_e32 v90, v90, v91
	v_mfma_f32_16x16x16_bf16 v[70:73], v[86:87], v[92:93], 0
	v_mov_b32_e32 v91, v90
	s_nop 1
	v_permlane32_swap_b32_e32 v90, v91
	v_add_f32_e32 v90, v90, v91
	v_rcp_f32_e32 v90, v90
	s_nop 2
	v_pk_mul_f32 v[70:71], v[70:71], v[90:91] op_sel_hi:[1,0]
	v_pk_mul_f32 v[72:73], v[72:73], v[90:91] op_sel_hi:[1,0]
	v_cvt_pk_bf16_f32 v120, v70, v71
	v_cvt_pk_bf16_f32 v121, v72, v73
	s_waitcnt lgkmcnt(0)
	v_mfma_f32_16x16x32_bf16 v[38:41], v[132:135], v[30:33], v[38:41]
	v_mfma_f32_16x16x32_bf16 v[46:49], v[140:143], v[30:33], v[46:49]
	v_mfma_f32_16x16x32_bf16 v[54:57], v[30:33], v[148:151], v[54:57]
	v_mfma_f32_16x16x32_bf16 v[38:41], v[136:139], v[34:37], v[38:41]
	v_mfma_f32_16x16x32_bf16 v[46:49], v[144:147], v[34:37], v[46:49]
	v_mfma_f32_16x16x32_bf16 v[54:57], v[34:37], v[154:157], v[54:57]
	ds_read_b128 v[132:135], v165 offset:4096
	ds_read_b128 v[136:139], v165 offset:5120
	ds_read_b128 v[140:143], v165 offset:12288
	ds_read_b128 v[144:147], v165 offset:13312
	ds_read_b128 v[148:151], v165 offset:20480
	ds_read_b128 v[154:157], v165 offset:21504
	s_nop 0
	v_cvt_pk_bf16_f32 v74, v38, v39
	v_cvt_pk_bf16_f32 v75, v40, v41
	v_cvt_pk_bf16_f32 v76, v46, v47
	v_cvt_pk_bf16_f32 v77, v48, v49
	ds_read_b128 v[38:41], v166 offset:128
	ds_read_b128 v[46:49], v166 offset:384
	v_mfma_f32_16x16x16_bf16 v[70:73], v[76:77], v[74:75], 0
	v_cvt_pk_bf16_f32 v86, v54, v55
	v_cvt_pk_bf16_f32 v87, v56, v57
	ds_read2_b32 v[54:55], v167 offset0:32 offset1:32
	ds_read2_b32 v[56:57], v167 offset0:32 offset1:32
	s_nop 3
	v_max_f32_e32 v88, v72, v73
	v_max3_f32 v88, v70, v71, v88
	v_cndmask_b32_e32 v88, v88, v94, vcc
	v_mov_b32_e32 v89, v88
	s_nop 1
	v_permlane16_swap_b32_e32 v88, v89
	v_max_f32_e32 v88, v88, v89
	v_mov_b32_e32 v89, v88
	s_nop 1
	v_permlane32_swap_b32_e32 v88, v89
	v_max_f32_e32 v88, v88, v89
	v_pk_add_f32 v[70:71], v[70:71], v[88:89] op_sel_hi:[1,0] neg_lo:[0,1] neg_hi:[0,1]
	v_pk_add_f32 v[72:73], v[72:73], v[88:89] op_sel_hi:[1,0] neg_lo:[0,1] neg_hi:[0,1]
	v_pk_mul_f32 v[70:71], v[62:63], v[70:71]
	v_pk_mul_f32 v[72:73], v[62:63], v[72:73]
	v_exp_f32_e32 v70, v70
	v_exp_f32_e32 v71, v71
	v_exp_f32_e32 v72, v72
	v_exp_f32_e32 v73, v73
	s_nop 0
	v_cndmask_b32_e64 v70, v70, 0, vcc
	v_cndmask_b32_e64 v71, v71, 0, vcc
	v_cndmask_b32_e64 v72, v72, 0, vcc
	v_cndmask_b32_e64 v73, v73, 0, vcc
	v_add_f32_e32 v90, v70, v71
	v_add_f32_e32 v91, v72, v73
	v_add_f32_e32 v90, v90, v91
	v_cvt_pk_bf16_f32 v92, v70, v71
	v_cvt_pk_bf16_f32 v93, v72, v73
	v_mov_b32_e32 v91, v90
	s_nop 1
	v_permlane16_swap_b32_e32 v90, v91
	v_add_f32_e32 v90, v90, v91
	v_mfma_f32_16x16x16_bf16 v[70:73], v[86:87], v[92:93], 0
	v_mov_b32_e32 v91, v90
	s_nop 1
	v_permlane32_swap_b32_e32 v90, v91
	v_add_f32_e32 v90, v90, v91
	v_rcp_f32_e32 v90, v90
	s_nop 2
	v_pk_mul_f32 v[70:71], v[70:71], v[90:91] op_sel_hi:[1,0]
	v_pk_mul_f32 v[72:73], v[72:73], v[90:91] op_sel_hi:[1,0]
	v_cvt_pk_bf16_f32 v122, v70, v71
	v_cvt_pk_bf16_f32 v123, v72, v73
	s_nop 1
	v_mfma_f32_16x16x32_bf16 v[42:45], v[96:99], v[120:123], v[42:45]
	v_mfma_f32_16x16x32_bf16 v[50:53], v[100:103], v[120:123], v[50:53]
	v_mfma_f32_16x16x32_bf16 v[58:61], v[104:107], v[120:123], v[58:61]
	v_mfma_f32_16x16x32_bf16 v[66:69], v[160:163], v[120:123], v[66:69]
	ds_read2st64_b64 v[96:99], v164 offset0:2 offset1:3
	ds_read2st64_b64 v[100:103], v164 offset0:6 offset1:7
	ds_read2st64_b64 v[104:107], v164 offset0:10 offset1:11
	ds_read2st64_b64 v[160:163], v164 offset0:14 offset1:15
	s_waitcnt lgkmcnt(4)
	v_mfma_f32_16x16x32_bf16 v[38:41], v[132:135], v[30:33], v[38:41]
	v_mfma_f32_16x16x32_bf16 v[46:49], v[140:143], v[30:33], v[46:49]
	v_mfma_f32_16x16x32_bf16 v[54:57], v[30:33], v[148:151], v[54:57]
	v_mfma_f32_16x16x32_bf16 v[38:41], v[136:139], v[34:37], v[38:41]
	v_mfma_f32_16x16x32_bf16 v[46:49], v[144:147], v[34:37], v[46:49]
	v_mfma_f32_16x16x32_bf16 v[54:57], v[34:37], v[154:157], v[54:57]
	ds_read_b128 v[132:135], v165 offset:6144
	ds_read_b128 v[136:139], v165 offset:7168
	ds_read_b128 v[140:143], v165 offset:14336
	ds_read_b128 v[144:147], v165 offset:15360
	ds_read_b128 v[148:151], v165 offset:22528
	ds_read_b128 v[154:157], v165 offset:23552
	s_nop 0
	v_cvt_pk_bf16_f32 v74, v38, v39
	v_cvt_pk_bf16_f32 v75, v40, v41
	v_cvt_pk_bf16_f32 v76, v46, v47
	v_cvt_pk_bf16_f32 v77, v48, v49
	ds_read_b128 v[38:41], v166 offset:192
	ds_read_b128 v[46:49], v166 offset:448
	v_mfma_f32_16x16x16_bf16 v[70:73], v[76:77], v[74:75], 0
	v_cvt_pk_bf16_f32 v86, v54, v55
	v_cvt_pk_bf16_f32 v87, v56, v57
	ds_read2_b32 v[54:55], v167 offset0:48 offset1:48
	ds_read2_b32 v[56:57], v167 offset0:48 offset1:48
	s_nop 3
	v_max_f32_e32 v88, v72, v73
	v_max3_f32 v88, v70, v71, v88
	v_cndmask_b32_e32 v88, v88, v94, vcc
	v_mov_b32_e32 v89, v88
	s_nop 1
	v_permlane16_swap_b32_e32 v88, v89
	v_max_f32_e32 v88, v88, v89
	v_mov_b32_e32 v89, v88
	s_nop 1
	v_permlane32_swap_b32_e32 v88, v89
	v_max_f32_e32 v88, v88, v89
	v_pk_add_f32 v[70:71], v[70:71], v[88:89] op_sel_hi:[1,0] neg_lo:[0,1] neg_hi:[0,1]
	v_pk_add_f32 v[72:73], v[72:73], v[88:89] op_sel_hi:[1,0] neg_lo:[0,1] neg_hi:[0,1]
	v_pk_mul_f32 v[70:71], v[62:63], v[70:71]
	v_pk_mul_f32 v[72:73], v[62:63], v[72:73]
	v_exp_f32_e32 v70, v70
	v_exp_f32_e32 v71, v71
	v_exp_f32_e32 v72, v72
	v_exp_f32_e32 v73, v73
	s_nop 0
	v_cndmask_b32_e64 v70, v70, 0, vcc
	v_cndmask_b32_e64 v71, v71, 0, vcc
	v_cndmask_b32_e64 v72, v72, 0, vcc
	v_cndmask_b32_e64 v73, v73, 0, vcc
	v_add_f32_e32 v90, v70, v71
	v_add_f32_e32 v91, v72, v73
	v_add_f32_e32 v90, v90, v91
	v_cvt_pk_bf16_f32 v92, v70, v71
	v_cvt_pk_bf16_f32 v93, v72, v73
	v_mov_b32_e32 v91, v90
	s_nop 1
	v_permlane16_swap_b32_e32 v90, v91
	v_add_f32_e32 v90, v90, v91
	v_mfma_f32_16x16x16_bf16 v[70:73], v[86:87], v[92:93], 0
	v_mov_b32_e32 v91, v90
	s_nop 1
	v_permlane32_swap_b32_e32 v90, v91
	v_add_f32_e32 v90, v90, v91
	v_rcp_f32_e32 v90, v90
	s_nop 2
	v_pk_mul_f32 v[70:71], v[70:71], v[90:91] op_sel_hi:[1,0]
	v_pk_mul_f32 v[72:73], v[72:73], v[90:91] op_sel_hi:[1,0]
	v_cvt_pk_bf16_f32 v120, v70, v71
	v_cvt_pk_bf16_f32 v121, v72, v73
	s_waitcnt lgkmcnt(0)
	v_mfma_f32_16x16x32_bf16 v[38:41], v[132:135], v[30:33], v[38:41]
	v_mfma_f32_16x16x32_bf16 v[46:49], v[140:143], v[30:33], v[46:49]
	v_mfma_f32_16x16x32_bf16 v[54:57], v[30:33], v[148:151], v[54:57]
	v_mfma_f32_16x16x32_bf16 v[38:41], v[136:139], v[34:37], v[38:41]
	v_mfma_f32_16x16x32_bf16 v[46:49], v[144:147], v[34:37], v[46:49]
	v_mfma_f32_16x16x32_bf16 v[54:57], v[34:37], v[154:157], v[54:57]
	s_nop 6
	v_cvt_pk_bf16_f32 v74, v38, v39
	v_cvt_pk_bf16_f32 v75, v40, v41
	v_cvt_pk_bf16_f32 v76, v46, v47
	v_cvt_pk_bf16_f32 v77, v48, v49
	s_nop 1
	v_mfma_f32_16x16x16_bf16 v[70:73], v[76:77], v[74:75], 0
	v_cvt_pk_bf16_f32 v86, v54, v55
	v_cvt_pk_bf16_f32 v87, v56, v57
	s_nop 5
	v_max_f32_e32 v88, v72, v73
	v_max3_f32 v88, v70, v71, v88
	v_cndmask_b32_e32 v88, v88, v94, vcc
	v_mov_b32_e32 v89, v88
	s_nop 1
	v_permlane16_swap_b32_e32 v88, v89
	v_max_f32_e32 v88, v88, v89
	v_mov_b32_e32 v89, v88
	s_nop 1
	v_permlane32_swap_b32_e32 v88, v89
	v_max_f32_e32 v88, v88, v89
	v_pk_add_f32 v[70:71], v[70:71], v[88:89] op_sel_hi:[1,0] neg_lo:[0,1] neg_hi:[0,1]
	v_pk_add_f32 v[72:73], v[72:73], v[88:89] op_sel_hi:[1,0] neg_lo:[0,1] neg_hi:[0,1]
	v_pk_mul_f32 v[70:71], v[62:63], v[70:71]
	v_pk_mul_f32 v[72:73], v[62:63], v[72:73]
	v_exp_f32_e32 v70, v70
	v_exp_f32_e32 v71, v71
	v_exp_f32_e32 v72, v72
	v_exp_f32_e32 v73, v73
	s_nop 0
	v_cndmask_b32_e64 v70, v70, 0, vcc
	v_cndmask_b32_e64 v71, v71, 0, vcc
	v_cndmask_b32_e64 v72, v72, 0, vcc
	v_cndmask_b32_e64 v73, v73, 0, vcc
	v_add_f32_e32 v90, v70, v71
	v_add_f32_e32 v91, v72, v73
	v_add_f32_e32 v90, v90, v91
	v_cvt_pk_bf16_f32 v92, v70, v71
	v_cvt_pk_bf16_f32 v93, v72, v73
	v_mov_b32_e32 v91, v90
	s_nop 1
	v_permlane16_swap_b32_e32 v90, v91
	v_add_f32_e32 v90, v90, v91
	v_mfma_f32_16x16x16_bf16 v[70:73], v[86:87], v[92:93], 0
	v_mov_b32_e32 v91, v90
	s_nop 1
	v_permlane32_swap_b32_e32 v90, v91
	v_add_f32_e32 v90, v90, v91
	v_rcp_f32_e32 v90, v90
	s_nop 2
	v_pk_mul_f32 v[70:71], v[70:71], v[90:91] op_sel_hi:[1,0]
	v_pk_mul_f32 v[72:73], v[72:73], v[90:91] op_sel_hi:[1,0]
	v_cvt_pk_bf16_f32 v122, v70, v71
	v_cvt_pk_bf16_f32 v123, v72, v73
	s_nop 1
	v_mfma_f32_16x16x32_bf16 v[42:45], v[96:99], v[120:123], v[42:45]
	v_mfma_f32_16x16x32_bf16 v[50:53], v[100:103], v[120:123], v[50:53]
	v_mfma_f32_16x16x32_bf16 v[58:61], v[104:107], v[120:123], v[58:61]
	v_mfma_f32_16x16x32_bf16 v[66:69], v[160:163], v[120:123], v[66:69]
	s_nop 1
	s_nop 3
	v_pk_add_f32 v[120:121], v[42:43], v[84:85]
	v_pk_add_f32 v[122:123], v[44:45], v[0:1]
	v_pk_add_f32 v[118:119], v[50:51], v[118:119]
	v_pk_add_f32 v[124:125], v[52:53], v[124:125]
	v_pk_add_f32 v[116:117], v[58:59], v[116:117]
	v_pk_add_f32 v[114:115], v[60:61], v[114:115]
	v_pk_add_f32 v[110:111], v[66:67], v[110:111]
	v_pk_add_f32 v[112:113], v[68:69], v[112:113]
	v_pk_mul_f32 v[30:31], v[120:121], v[120:121]
	v_pk_add_f32 v[32:33], v[120:121], v[122:123]
	v_pk_fma_f32 v[30:31], v[122:123], v[122:123], v[30:31]
	v_pk_add_f32 v[32:33], v[32:33], v[118:119]
	v_pk_fma_f32 v[30:31], v[118:119], v[118:119], v[30:31]
	v_pk_add_f32 v[32:33], v[32:33], v[124:125]
	v_pk_fma_f32 v[30:31], v[124:125], v[124:125], v[30:31]
	v_pk_add_f32 v[32:33], v[32:33], v[116:117]
	v_pk_fma_f32 v[30:31], v[116:117], v[116:117], v[30:31]
	v_pk_add_f32 v[32:33], v[32:33], v[114:115]
	v_pk_fma_f32 v[30:31], v[114:115], v[114:115], v[30:31]
	v_pk_add_f32 v[32:33], v[32:33], v[110:111]
	v_pk_fma_f32 v[30:31], v[110:111], v[110:111], v[30:31]
	v_pk_add_f32 v[32:33], v[32:33], v[112:113]
	v_pk_fma_f32 v[30:31], v[112:113], v[112:113], v[30:31]
	v_add_f32_e32 v0, v30, v31
	v_add_f32_e32 v1, v32, v33
	v_mul_f32_e32 v0, v130, v0
	v_mul_f32_e32 v1, v130, v1
	s_branch .LBB5_139

.LBB5_172:
	s_and_b64 vcc, exec, s[0:1]
	v_mov_b32_e32 v24, 0
	s_waitcnt lgkmcnt(0)
	s_barrier
	s_cbranch_vccnz .LBB5_174
	v_mov_b32_e32 v68, 0x23e90
	ds_read_b64 v[126:127], v68
	v_mov_b32_e32 v68, 0xb000
	v_lshl_or_b32 v136, v128, 4, v68
	v_or_b32_e32 v137, 0x23400, v131
	s_waitcnt vmcnt(0)
	ds_read_b128 v[0:3], v137 offset:1024
	ds_read_b128 v[4:7], v137 offset:1088
	ds_read_b128 v[8:11], v137 offset:1152
	ds_read_b128 v[12:15], v137 offset:1216
	ds_read_b128 v[20:23], v137
	ds_read_b128 v[24:27], v137 offset:64
	ds_read_b128 v[36:39], v136
	ds_read_b128 v[40:43], v136 offset:1024
	ds_read_b128 v[44:47], v136 offset:2048
	ds_read_b128 v[48:51], v136 offset:3072
	s_waitcnt lgkmcnt(10)
	v_pk_add_f32 v[68:69], v[120:121], v[126:127] op_sel_hi:[1,0] neg_lo:[0,1] neg_hi:[0,1]
	v_pk_mul_f32 v[68:69], v[126:127], v[68:69] op_sel:[1,0]
	v_pk_fma_f32 v[84:85], v[70:71], v[68:69], v[102:103]
	v_pk_add_f32 v[68:69], v[122:123], v[126:127] op_sel_hi:[1,0] neg_lo:[0,1] neg_hi:[0,1]
	v_pk_mul_f32 v[68:69], v[126:127], v[68:69] op_sel:[1,0]
	v_pk_fma_f32 v[102:103], v[72:73], v[68:69], v[104:105]
	v_pk_add_f32 v[68:69], v[118:119], v[126:127] op_sel_hi:[1,0] neg_lo:[0,1] neg_hi:[0,1]
	v_pk_mul_f32 v[68:69], v[126:127], v[68:69] op_sel:[1,0]
	v_pk_fma_f32 v[104:105], v[74:75], v[68:69], v[106:107]
	v_pk_add_f32 v[68:69], v[124:125], v[126:127] op_sel_hi:[1,0] neg_lo:[0,1] neg_hi:[0,1]
	v_pk_mul_f32 v[68:69], v[126:127], v[68:69] op_sel:[1,0]
	v_pk_fma_f32 v[106:107], v[76:77], v[68:69], v[108:109]
	v_cvt_pk_bf16_f32 v120, v84, v85
	v_cvt_pk_bf16_f32 v121, v102, v103
	v_cvt_pk_bf16_f32 v122, v104, v105
	v_cvt_pk_bf16_f32 v123, v106, v107
	v_pk_add_f32 v[68:69], v[116:117], v[126:127] op_sel_hi:[1,0] neg_lo:[0,1] neg_hi:[0,1]
	v_pk_mul_f32 v[68:69], v[126:127], v[68:69] op_sel:[1,0]
	v_pk_fma_f32 v[86:87], v[96:97], v[68:69], v[86:87]
	v_pk_add_f32 v[68:69], v[114:115], v[126:127] op_sel_hi:[1,0] neg_lo:[0,1] neg_hi:[0,1]
	v_pk_mul_f32 v[68:69], v[126:127], v[68:69] op_sel:[1,0]
	v_pk_fma_f32 v[88:89], v[152:153], v[68:69], v[88:89]
	v_pk_add_f32 v[68:69], v[110:111], v[126:127] op_sel_hi:[1,0] neg_lo:[0,1] neg_hi:[0,1]
	v_pk_mul_f32 v[68:69], v[126:127], v[68:69] op_sel:[1,0]
	v_pk_fma_f32 v[90:91], v[90:91], v[68:69], v[98:99]
	v_pk_add_f32 v[68:69], v[112:113], v[126:127] op_sel_hi:[1,0] neg_lo:[0,1] neg_hi:[0,1]
	v_pk_mul_f32 v[68:69], v[126:127], v[68:69] op_sel:[1,0]
	v_pk_fma_f32 v[92:93], v[92:93], v[68:69], v[100:101]
	v_cvt_pk_bf16_f32 v16, v86, v87
	v_cvt_pk_bf16_f32 v17, v88, v89
	v_cvt_pk_bf16_f32 v18, v90, v91
	v_cvt_pk_bf16_f32 v19, v92, v93
	ds_read_b128 v[28:31], v137 offset:128
	ds_read_b128 v[32:35], v137 offset:192
	ds_read_b128 v[52:55], v136 offset:32768
	ds_read_b128 v[56:59], v136 offset:40960
	ds_read_b128 v[60:63], v136 offset:49152
	ds_read_b128 v[64:67], v136 offset:57344
	s_waitcnt lgkmcnt(6)
	v_mfma_f32_16x16x32_bf16 v[20:23], v[36:39], v[120:123], v[20:23]
	v_mfma_f32_16x16x32_bf16 v[24:27], v[44:47], v[120:123], v[24:27]
	v_mfma_f32_16x16x32_bf16 v[20:23], v[40:43], v[16:19], v[20:23]
	v_mfma_f32_16x16x32_bf16 v[24:27], v[48:51], v[16:19], v[24:27]
	ds_read_b128 v[36:39], v136 offset:4096
	ds_read_b128 v[40:43], v136 offset:5120
	ds_read_b128 v[44:47], v136 offset:6144
	ds_read_b128 v[48:51], v136 offset:7168
	s_waitcnt lgkmcnt(0)
	v_mfma_f32_16x16x32_bf16 v[28:31], v[36:39], v[120:123], v[28:31]
	v_mfma_f32_16x16x32_bf16 v[32:35], v[44:47], v[120:123], v[32:35]
	v_mfma_f32_16x16x32_bf16 v[28:31], v[40:43], v[16:19], v[28:31]
	v_mfma_f32_16x16x32_bf16 v[32:35], v[48:51], v[16:19], v[32:35]
	ds_read_b128 v[36:39], v136 offset:8192
	ds_read_b128 v[40:43], v136 offset:9216
	ds_read_b128 v[44:47], v136 offset:10240
	ds_read_b128 v[48:51], v136 offset:11264
	v_max_f32_e32 v20, 0, v20
	v_max_f32_e32 v21, 0, v21
	v_max_f32_e32 v22, 0, v22
	v_max_f32_e32 v23, 0, v23
	v_max_f32_e32 v24, 0, v24
	v_max_f32_e32 v25, 0, v25
	v_max_f32_e32 v26, 0, v26
	v_max_f32_e32 v27, 0, v27
	v_cvt_pk_bf16_f32 v132, v20, v21
	v_cvt_pk_bf16_f32 v133, v22, v23
	v_cvt_pk_bf16_f32 v134, v24, v25
	v_cvt_pk_bf16_f32 v135, v26, v27
	ds_read_b128 v[20:23], v137 offset:256
	ds_read_b128 v[24:27], v137 offset:320
	v_mfma_f32_16x16x32_bf16 v[0:3], v[52:55], v[132:135], v[0:3]
	v_mfma_f32_16x16x32_bf16 v[4:7], v[56:59], v[132:135], v[4:7]
	v_mfma_f32_16x16x32_bf16 v[8:11], v[60:63], v[132:135], v[8:11]
	v_mfma_f32_16x16x32_bf16 v[12:15], v[64:67], v[132:135], v[12:15]
	ds_read_b128 v[52:55], v136 offset:33792
	ds_read_b128 v[56:59], v136 offset:41984
	ds_read_b128 v[60:63], v136 offset:50176
	ds_read_b128 v[64:67], v136 offset:58368
	s_waitcnt lgkmcnt(4)
	v_mfma_f32_16x16x32_bf16 v[20:23], v[36:39], v[120:123], v[20:23]
	v_mfma_f32_16x16x32_bf16 v[24:27], v[44:47], v[120:123], v[24:27]
	v_mfma_f32_16x16x32_bf16 v[20:23], v[40:43], v[16:19], v[20:23]
	v_mfma_f32_16x16x32_bf16 v[24:27], v[48:51], v[16:19], v[24:27]
	ds_read_b128 v[36:39], v136 offset:12288
	ds_read_b128 v[40:43], v136 offset:13312
	ds_read_b128 v[44:47], v136 offset:14336
	ds_read_b128 v[48:51], v136 offset:15360
	v_max_f32_e32 v28, 0, v28
	v_max_f32_e32 v29, 0, v29
	v_max_f32_e32 v30, 0, v30
	v_max_f32_e32 v31, 0, v31
	v_max_f32_e32 v32, 0, v32
	v_max_f32_e32 v33, 0, v33
	v_max_f32_e32 v34, 0, v34
	v_max_f32_e32 v35, 0, v35
	v_cvt_pk_bf16_f32 v132, v28, v29
	v_cvt_pk_bf16_f32 v133, v30, v31
	v_cvt_pk_bf16_f32 v134, v32, v33
	v_cvt_pk_bf16_f32 v135, v34, v35
	ds_read_b128 v[28:31], v137 offset:384
	ds_read_b128 v[32:35], v137 offset:448
	s_waitcnt lgkmcnt(6)
	v_mfma_f32_16x16x32_bf16 v[0:3], v[52:55], v[132:135], v[0:3]
	v_mfma_f32_16x16x32_bf16 v[4:7], v[56:59], v[132:135], v[4:7]
	v_mfma_f32_16x16x32_bf16 v[8:11], v[60:63], v[132:135], v[8:11]
	v_mfma_f32_16x16x32_bf16 v[12:15], v[64:67], v[132:135], v[12:15]
	ds_read_b128 v[52:55], v136 offset:34816
	ds_read_b128 v[56:59], v136 offset:43008
	ds_read_b128 v[60:63], v136 offset:51200
	ds_read_b128 v[64:67], v136 offset:59392
	s_waitcnt lgkmcnt(4)
	v_mfma_f32_16x16x32_bf16 v[28:31], v[36:39], v[120:123], v[28:31]
	v_mfma_f32_16x16x32_bf16 v[32:35], v[44:47], v[120:123], v[32:35]
	v_mfma_f32_16x16x32_bf16 v[28:31], v[40:43], v[16:19], v[28:31]
	v_mfma_f32_16x16x32_bf16 v[32:35], v[48:51], v[16:19], v[32:35]
	ds_read_b128 v[36:39], v136 offset:16384
	ds_read_b128 v[40:43], v136 offset:17408
	ds_read_b128 v[44:47], v136 offset:18432
	ds_read_b128 v[48:51], v136 offset:19456
	v_max_f32_e32 v20, 0, v20
	v_max_f32_e32 v21, 0, v21
	v_max_f32_e32 v22, 0, v22
	v_max_f32_e32 v23, 0, v23
	v_max_f32_e32 v24, 0, v24
	v_max_f32_e32 v25, 0, v25
	v_max_f32_e32 v26, 0, v26
	v_max_f32_e32 v27, 0, v27
	v_cvt_pk_bf16_f32 v132, v20, v21
	v_cvt_pk_bf16_f32 v133, v22, v23
	v_cvt_pk_bf16_f32 v134, v24, v25
	v_cvt_pk_bf16_f32 v135, v26, v27
	ds_read_b128 v[20:23], v137 offset:512
	ds_read_b128 v[24:27], v137 offset:576
	s_waitcnt lgkmcnt(6)
	v_mfma_f32_16x16x32_bf16 v[0:3], v[52:55], v[132:135], v[0:3]
	v_mfma_f32_16x16x32_bf16 v[4:7], v[56:59], v[132:135], v[4:7]
	v_mfma_f32_16x16x32_bf16 v[8:11], v[60:63], v[132:135], v[8:11]
	v_mfma_f32_16x16x32_bf16 v[12:15], v[64:67], v[132:135], v[12:15]
	ds_read_b128 v[52:55], v136 offset:35840
	ds_read_b128 v[56:59], v136 offset:44032
	ds_read_b128 v[60:63], v136 offset:52224
	ds_read_b128 v[64:67], v136 offset:60416
	s_waitcnt lgkmcnt(4)
	v_mfma_f32_16x16x32_bf16 v[20:23], v[36:39], v[120:123], v[20:23]
	v_mfma_f32_16x16x32_bf16 v[24:27], v[44:47], v[120:123], v[24:27]
	v_mfma_f32_16x16x32_bf16 v[20:23], v[40:43], v[16:19], v[20:23]
	v_mfma_f32_16x16x32_bf16 v[24:27], v[48:51], v[16:19], v[24:27]
	ds_read_b128 v[36:39], v136 offset:20480
	ds_read_b128 v[40:43], v136 offset:21504
	ds_read_b128 v[44:47], v136 offset:22528
	ds_read_b128 v[48:51], v136 offset:23552
	v_max_f32_e32 v28, 0, v28
	v_max_f32_e32 v29, 0, v29
	v_max_f32_e32 v30, 0, v30
	v_max_f32_e32 v31, 0, v31
	v_max_f32_e32 v32, 0, v32
	v_max_f32_e32 v33, 0, v33
	v_max_f32_e32 v34, 0, v34
	v_max_f32_e32 v35, 0, v35
	v_cvt_pk_bf16_f32 v132, v28, v29
	v_cvt_pk_bf16_f32 v133, v30, v31
	v_cvt_pk_bf16_f32 v134, v32, v33
	v_cvt_pk_bf16_f32 v135, v34, v35
	ds_read_b128 v[28:31], v137 offset:640
	ds_read_b128 v[32:35], v137 offset:704
	s_waitcnt lgkmcnt(6)
	v_mfma_f32_16x16x32_bf16 v[0:3], v[52:55], v[132:135], v[0:3]
	v_mfma_f32_16x16x32_bf16 v[4:7], v[56:59], v[132:135], v[4:7]
	v_mfma_f32_16x16x32_bf16 v[8:11], v[60:63], v[132:135], v[8:11]
	v_mfma_f32_16x16x32_bf16 v[12:15], v[64:67], v[132:135], v[12:15]
	ds_read_b128 v[52:55], v136 offset:36864
	ds_read_b128 v[56:59], v136 offset:45056
	ds_read_b128 v[60:63], v136 offset:53248
	ds_read_b128 v[64:67], v136 offset:61440
	s_waitcnt lgkmcnt(4)
	v_mfma_f32_16x16x32_bf16 v[28:31], v[36:39], v[120:123], v[28:31]
	v_mfma_f32_16x16x32_bf16 v[32:35], v[44:47], v[120:123], v[32:35]
	v_mfma_f32_16x16x32_bf16 v[28:31], v[40:43], v[16:19], v[28:31]
	v_mfma_f32_16x16x32_bf16 v[32:35], v[48:51], v[16:19], v[32:35]
	ds_read_b128 v[36:39], v136 offset:24576
	ds_read_b128 v[40:43], v136 offset:25600
	ds_read_b128 v[44:47], v136 offset:26624
	ds_read_b128 v[48:51], v136 offset:27648
	v_max_f32_e32 v20, 0, v20
	v_max_f32_e32 v21, 0, v21
	v_max_f32_e32 v22, 0, v22
	v_max_f32_e32 v23, 0, v23
	v_max_f32_e32 v24, 0, v24
	v_max_f32_e32 v25, 0, v25
	v_max_f32_e32 v26, 0, v26
	v_max_f32_e32 v27, 0, v27
	v_cvt_pk_bf16_f32 v132, v20, v21
	v_cvt_pk_bf16_f32 v133, v22, v23
	v_cvt_pk_bf16_f32 v134, v24, v25
	v_cvt_pk_bf16_f32 v135, v26, v27
	ds_read_b128 v[20:23], v137 offset:768
	ds_read_b128 v[24:27], v137 offset:832
	s_waitcnt lgkmcnt(6)
	v_mfma_f32_16x16x32_bf16 v[0:3], v[52:55], v[132:135], v[0:3]
	v_mfma_f32_16x16x32_bf16 v[4:7], v[56:59], v[132:135], v[4:7]
	v_mfma_f32_16x16x32_bf16 v[8:11], v[60:63], v[132:135], v[8:11]
	v_mfma_f32_16x16x32_bf16 v[12:15], v[64:67], v[132:135], v[12:15]
	ds_read_b128 v[52:55], v136 offset:37888
	ds_read_b128 v[56:59], v136 offset:46080
	ds_read_b128 v[60:63], v136 offset:54272
	ds_read_b128 v[64:67], v136 offset:62464
	s_waitcnt lgkmcnt(4)
	v_mfma_f32_16x16x32_bf16 v[20:23], v[36:39], v[120:123], v[20:23]
	v_mfma_f32_16x16x32_bf16 v[24:27], v[44:47], v[120:123], v[24:27]
	v_mfma_f32_16x16x32_bf16 v[20:23], v[40:43], v[16:19], v[20:23]
	v_mfma_f32_16x16x32_bf16 v[24:27], v[48:51], v[16:19], v[24:27]
	ds_read_b128 v[36:39], v136 offset:28672
	ds_read_b128 v[40:43], v136 offset:29696
	ds_read_b128 v[44:47], v136 offset:30720
	ds_read_b128 v[48:51], v136 offset:31744
	v_max_f32_e32 v28, 0, v28
	v_max_f32_e32 v29, 0, v29
	v_max_f32_e32 v30, 0, v30
	v_max_f32_e32 v31, 0, v31
	v_max_f32_e32 v32, 0, v32
	v_max_f32_e32 v33, 0, v33
	v_max_f32_e32 v34, 0, v34
	v_max_f32_e32 v35, 0, v35
	v_cvt_pk_bf16_f32 v132, v28, v29
	v_cvt_pk_bf16_f32 v133, v30, v31
	v_cvt_pk_bf16_f32 v134, v32, v33
	v_cvt_pk_bf16_f32 v135, v34, v35
	ds_read_b128 v[28:31], v137 offset:896
	ds_read_b128 v[32:35], v137 offset:960
	s_waitcnt lgkmcnt(6)
	v_mfma_f32_16x16x32_bf16 v[0:3], v[52:55], v[132:135], v[0:3]
	v_mfma_f32_16x16x32_bf16 v[4:7], v[56:59], v[132:135], v[4:7]
	v_mfma_f32_16x16x32_bf16 v[8:11], v[60:63], v[132:135], v[8:11]
	v_mfma_f32_16x16x32_bf16 v[12:15], v[64:67], v[132:135], v[12:15]
	ds_read_b128 v[52:55], v136 offset:38912
	ds_read_b128 v[56:59], v136 offset:47104
	ds_read_b128 v[60:63], v136 offset:55296
	ds_read_b128 v[64:67], v136 offset:63488
	s_waitcnt lgkmcnt(4)
	v_mfma_f32_16x16x32_bf16 v[28:31], v[36:39], v[120:123], v[28:31]
	v_mfma_f32_16x16x32_bf16 v[32:35], v[44:47], v[120:123], v[32:35]
	v_mfma_f32_16x16x32_bf16 v[28:31], v[40:43], v[16:19], v[28:31]
	v_mfma_f32_16x16x32_bf16 v[32:35], v[48:51], v[16:19], v[32:35]
	s_nop 3
	v_max_f32_e32 v20, 0, v20
	v_max_f32_e32 v21, 0, v21
	v_max_f32_e32 v22, 0, v22
	v_max_f32_e32 v23, 0, v23
	v_max_f32_e32 v24, 0, v24
	v_max_f32_e32 v25, 0, v25
	v_max_f32_e32 v26, 0, v26
	v_max_f32_e32 v27, 0, v27
	v_cvt_pk_bf16_f32 v132, v20, v21
	v_cvt_pk_bf16_f32 v133, v22, v23
	v_cvt_pk_bf16_f32 v134, v24, v25
	v_cvt_pk_bf16_f32 v135, v26, v27
	s_nop 1
	s_waitcnt lgkmcnt(0)
	v_mfma_f32_16x16x32_bf16 v[0:3], v[52:55], v[132:135], v[0:3]
	v_mfma_f32_16x16x32_bf16 v[4:7], v[56:59], v[132:135], v[4:7]
	v_mfma_f32_16x16x32_bf16 v[8:11], v[60:63], v[132:135], v[8:11]
	v_mfma_f32_16x16x32_bf16 v[12:15], v[64:67], v[132:135], v[12:15]
	ds_read_b128 v[52:55], v136 offset:39936
	ds_read_b128 v[56:59], v136 offset:48128
	ds_read_b128 v[60:63], v136 offset:56320
	ds_read_b128 v[64:67], v136 offset:64512
	s_nop 7
	v_max_f32_e32 v28, 0, v28
	v_max_f32_e32 v29, 0, v29
	v_max_f32_e32 v30, 0, v30
	v_max_f32_e32 v31, 0, v31
	v_max_f32_e32 v32, 0, v32
	v_max_f32_e32 v33, 0, v33
	v_max_f32_e32 v34, 0, v34
	v_max_f32_e32 v35, 0, v35
	v_cvt_pk_bf16_f32 v132, v28, v29
	v_cvt_pk_bf16_f32 v133, v30, v31
	v_cvt_pk_bf16_f32 v134, v32, v33
	v_cvt_pk_bf16_f32 v135, v34, v35
	s_nop 1
	s_waitcnt lgkmcnt(0)
	v_mfma_f32_16x16x32_bf16 v[0:3], v[52:55], v[132:135], v[0:3]
	v_mfma_f32_16x16x32_bf16 v[4:7], v[56:59], v[132:135], v[4:7]
	v_mfma_f32_16x16x32_bf16 v[8:11], v[60:63], v[132:135], v[8:11]
	v_mfma_f32_16x16x32_bf16 v[12:15], v[64:67], v[132:135], v[12:15]
	s_nop 4
	v_pk_add_f32 v[120:121], v[0:1], v[84:85]
	v_pk_add_f32 v[122:123], v[2:3], v[102:103]
	v_pk_add_f32 v[118:119], v[4:5], v[104:105]
	v_pk_add_f32 v[124:125], v[6:7], v[106:107]
	v_pk_add_f32 v[116:117], v[8:9], v[86:87]
	v_pk_add_f32 v[114:115], v[10:11], v[88:89]
	v_pk_add_f32 v[110:111], v[12:13], v[90:91]
	v_pk_add_f32 v[112:113], v[14:15], v[92:93]
	v_pk_mul_f32 v[36:37], v[120:121], v[120:121]
	v_pk_add_f32 v[38:39], v[120:121], v[122:123]
	v_pk_fma_f32 v[36:37], v[122:123], v[122:123], v[36:37]
	v_pk_add_f32 v[38:39], v[38:39], v[118:119]
	v_pk_fma_f32 v[36:37], v[118:119], v[118:119], v[36:37]
	v_pk_add_f32 v[38:39], v[38:39], v[124:125]
	v_pk_fma_f32 v[36:37], v[124:125], v[124:125], v[36:37]
	v_pk_add_f32 v[38:39], v[38:39], v[116:117]
	v_pk_fma_f32 v[36:37], v[116:117], v[116:117], v[36:37]
	v_pk_add_f32 v[38:39], v[38:39], v[114:115]
	v_pk_fma_f32 v[36:37], v[114:115], v[114:115], v[36:37]
	v_pk_add_f32 v[38:39], v[38:39], v[110:111]
	v_pk_fma_f32 v[36:37], v[110:111], v[110:111], v[36:37]
	v_pk_add_f32 v[38:39], v[38:39], v[112:113]
	v_pk_fma_f32 v[36:37], v[112:113], v[112:113], v[36:37]
	v_add_f32_e32 v24, v36, v37
	v_add_f32_e32 v25, v38, v39
	v_mul_f32_e32 v24, v130, v24
	v_mul_f32_e32 v25, v130, v25
	s_branch .LBB5_175
